# stack of exact latency edits on v56: local-barrier leader releases without waiting for its own invalidate, attention item setup loads batched, conversion header scalar loads waited once
# baseline (speedup 1.0000x reference)
.Lknown_seam5:
	s_cmp_eq_u32 s10, 2
	s_cbranch_scc0 .Lfull_seam5
	v_mov_b32_e32 v0, 0x2000
	global_atomic_add v0, v239, s[6:7] offset:1024
	s_waitcnt vmcnt(0)
	s_branch .LBB0_1134

.LBB0_1716:
	s_andn2_saveexec_b64 s[8:9], s[8:9]
	s_cbranch_execnz .LBB0_1717
.Lloc_far11b:
	s_getpc_b64 s[98:99]
